# combination variant with 1040 weight blocks in the layer-1 MoE down-projection tail and a lighter layer-2 merge tail
# baseline (speedup 1.0000x reference)
.LBB0_109:
	v_readlane_b32 s0, v251, 5
	v_readlane_b32 s6, v251, 11
	v_readlane_b32 s7, v251, 12
	s_add_u32 s0, s6, 0x10f00000
	v_writelane_b32 v252, s0, 12
	s_addc_u32 s0, s7, 0
	v_writelane_b32 v252, s0, 13
	s_add_u32 s0, s6, 0x3c90c0
	v_writelane_b32 v252, s0, 14
	s_addc_u32 s0, s7, 0
	v_writelane_b32 v252, s0, 15
	s_add_u32 s0, s6, 0x3ad0c0
	v_writelane_b32 v252, s0, 16
	s_addc_u32 s0, s7, 0
	v_writelane_b32 v252, s0, 17
	s_add_u32 s0, s6, 0x13800000
	v_writelane_b32 v252, s0, 18
	s_addc_u32 s0, s7, 0
	v_writelane_b32 v252, s0, 19
	s_add_u32 s0, s6, 0x33d0c0
	v_writelane_b32 v252, s0, 20
	s_addc_u32 s0, s7, 0
	v_writelane_b32 v252, s0, 21
	s_add_u32 s0, s6, 0x11700000
	v_writelane_b32 v252, s0, 22
	s_addc_u32 s0, s7, 0
	v_writelane_b32 v252, s0, 23
	s_add_u32 s0, s6, 0x3320c0
	v_mov_b32_e32 v0, 0x135f
	v_readlane_b32 s1, v251, 6
	v_writelane_b32 v252, s0, 24
	s_addc_u32 s0, s7, 0
	v_cmp_gt_i32_e32 vcc, s28, v0
	v_readlane_b32 s2, v251, 7
	v_readlane_b32 s3, v251, 8
	v_readlane_b32 s4, v251, 9
	v_readlane_b32 s5, v251, 10
	v_writelane_b32 v252, s0, 25
	s_and_b64 s[0:1], vcc, exec
	s_mov_b64 s[0:1], s[52:53]
	s_mov_b64 s[2:3], s[54:55]
	s_mov_b64 s[4:5], s[56:57]
	s_mov_b64 s[6:7], s[58:59]
	s_mov_b64 s[8:9], s[60:61]
	s_mov_b64 s[10:11], s[62:63]
	s_mov_b64 s[12:13], s[64:65]
	v_writelane_b32 v252, s0, 26
	s_waitcnt lgkmcnt(0)
	s_barrier
	v_writelane_b32 v252, s1, 27
	v_writelane_b32 v252, s2, 28
	v_writelane_b32 v252, s3, 29
	v_writelane_b32 v252, s4, 30
	v_writelane_b32 v252, s5, 31
	v_writelane_b32 v252, s6, 32
	v_writelane_b32 v252, s7, 33
	v_writelane_b32 v252, s8, 34
	v_writelane_b32 v252, s9, 35
	v_writelane_b32 v252, s10, 36
	v_writelane_b32 v252, s11, 37
	v_writelane_b32 v252, s12, 38
	v_writelane_b32 v252, s13, 39
	v_writelane_b32 v252, s14, 40
	v_writelane_b32 v252, s15, 41
	s_cbranch_scc1 .LBB0_253
	s_mov_b32 s98, s28
	v_readlane_b32 s100, v251, 24
	s_movk_i32 s99, 0xe0
	s_mov_b32 s101, 0
	s_mov_b32 s0, 0xfffffc00
	s_cmp_lt_u32 s98, 0x1278
	s_cselect_b32 s0, 0xfffffc00, s0
	s_cmp_lt_u32 s98, 0x11d0
	s_cselect_b32 s0, 0xfffffc00, s0
	s_cmp_lt_u32 s98, 0x10e0
	s_cselect_b32 s0, 0xfffffc00, s0
	s_cmp_lt_u32 s98, 0x1010
	s_cselect_b32 s0, 0xfffffc00, s0
	s_cmp_lt_u32 s98, 0xc60
	s_cselect_b32 s0, 0x700, s0
	s_cmp_lt_u32 s98, 0xc40
	s_cselect_b32 s0, 0x6a0, s0
	s_cmp_lt_u32 s98, 0xc00
	s_cselect_b32 s0, 0x6a0, s0
	s_cmp_lt_u32 s98, 0xb60
	s_cselect_b32 s0, 0xfffff600, s0
	s_cmp_lt_u32 s98, 0xab0
	s_cselect_b32 s0, 0x890, s0
	s_cmp_lt_u32 s98, 0xa90
	s_cselect_b32 s0, 0x770, s0
	s_cmp_lt_u32 s98, 0xa20
	s_cselect_b32 s0, 0x770, s0
	s_cmp_lt_u32 s98, 0x9b0
	s_cselect_b32 s0, 0xfffffeb0, s0
	s_cmp_lt_u32 s98, 0x880
	s_cselect_b32 s0, 0xfffffeb0, s0
	s_cmp_lt_u32 s98, 0x5b0
	s_cselect_b32 s0, 0xfffffeb0, s0
	s_cmp_lt_u32 s98, 0x460
	s_cselect_b32 s0, 0xfffffeb0, s0
	s_cmp_lt_u32 s98, 0x2b0
	s_cselect_b32 s0, 0x1070, s0
	s_cmp_lt_u32 s98, 0x290
	s_cselect_b32 s0, 0xe90, s0
	s_cmp_lt_u32 s98, 0x280
	s_cselect_b32 s0, 0xe90, s0
	s_cmp_lt_u32 s98, 0x1b0
	s_cselect_b32 s0, 0xffffff00, s0
	s_cmp_lt_u32 s98, 0x100
	s_cselect_b32 s0, 0x1200, s0
	s_cmp_lt_u32 s98, 0xe0
	s_cselect_b32 s0, 0xf60, s0
	s_add_i32 s28, s98, s0
	v_lshlrev_b32_e32 v0, 2, v50
	s_add_i32 s0, 0, 0x21000
	v_and_b32_e32 v37, 31, v50
	v_add_u32_e32 v39, s0, v0
	v_cmp_gt_i32_e64 s[0:1], 32, v50
	v_lshlrev_b32_e32 v1, 1, v50
	v_lshlrev_b32_e32 v42, 2, v37
	v_writelane_b32 v252, s0, 42
	v_ashrrev_i32_e32 v40, 3, v50
	v_and_b32_e32 v2, 0xffffffc0, v1
	v_add_u32_e32 v4, 0, v42
	v_writelane_b32 v252, s1, 43
	s_add_i32 s0, 0, 0x21800
	s_movk_i32 s2, 0x84
	v_and_b32_e32 v45, 7, v50
	v_add_u32_e32 v43, s0, v0
	v_add_u32_e32 v82, s0, v42
	v_mad_u64_u32 v[6:7], s[0:1], v2, s2, v[4:5]
	v_mul_lo_u32 v41, v40, s2
	v_lshlrev_b32_e32 v45, 4, v45
	v_add3_u32 v83, v41, v45, 0
	v_lshrrev_b32_e32 v45, 5, v50
	s_movk_i32 s0, 0x2100
	v_and_b32_e32 v35, 28, v0
	v_or_b32_e32 v0, 62, v1
	v_or_b32_e32 v1, 63, v1
	v_mul_lo_u32 v84, v45, s0
	v_mul_lo_u32 v0, v0, s2
	v_mul_lo_u32 v44, v1, s2
	v_or_b32_e32 v10, 2, v2
	v_or_b32_e32 v12, 4, v2
	v_or_b32_e32 v14, 6, v2
	v_or_b32_e32 v16, 8, v2
	v_or_b32_e32 v18, 10, v2
	v_or_b32_e32 v20, 12, v2
	v_or_b32_e32 v22, 14, v2
	v_or_b32_e32 v24, 16, v2
	v_or_b32_e32 v26, 18, v2
	v_or_b32_e32 v28, 20, v2
	v_or_b32_e32 v30, 22, v2
	v_or_b32_e32 v32, 24, v2
	v_or_b32_e32 v34, 26, v2
	v_or_b32_e32 v36, 28, v2
	v_or_b32_e32 v38, 30, v2
	v_ashrrev_i32_e32 v41, 31, v40
	v_or_b32_e32 v42, v84, v42
	v_ashrrev_i32_e32 v3, 31, v2
	v_mov_b32_e32 v8, v2
	v_mov_b32_e32 v1, v2
	v_mov_b32_e32 v5, v10
	v_mov_b32_e32 v7, v12
	v_mov_b32_e32 v9, v14
	v_mov_b32_e32 v11, v16
	v_mov_b32_e32 v13, v18
	v_mov_b32_e32 v15, v20
	v_mov_b32_e32 v17, v22
	v_mov_b32_e32 v19, v24
	v_mov_b32_e32 v21, v26
	v_mov_b32_e32 v23, v28
	v_mov_b32_e32 v25, v30
	v_mov_b32_e32 v27, v32
	v_mov_b32_e32 v29, v34
	v_mov_b32_e32 v31, v36
	v_mov_b32_e32 v33, v38
	v_lshlrev_b64 v[40:41], 2, v[40:41]
	v_add_u32_e32 v42, 0, v42
	v_mov_b32_e32 v45, 0
	v_add_u32_e32 v85, v4, v0
	v_add_u32_e32 v86, v4, v44
	s_branch .LBB0_112
.LBB0_111:
	s_or_b64 exec, exec, s[0:1]
	s_waitcnt lgkmcnt(0)
	s_barrier
	ds_read_b32 v0, v82
	ds_read_b32 v44, v85
	ds_read_b32 v58, v86
	s_mov_b32 s2, 0x42fe0000
	v_add_u32_e32 v57, 0x400, v6
	s_waitcnt lgkmcnt(2)
	v_div_scale_f32 v46, s[0:1], v0, v0, s2
	v_rcp_f32_e32 v47, v46
	v_readlane_b32 s0, v252, 46
	v_readlane_b32 s1, v252, 47
	v_add_u32_e32 v60, 0x800, v6
	v_fma_f32 v48, -v46, v47, 1.0
	v_fmac_f32_e32 v47, v48, v47
	v_div_scale_f32 v48, vcc, s2, v0, s2
	v_mul_f32_e32 v49, v48, v47
	v_fma_f32 v52, -v46, v49, v48
	v_fmac_f32_e32 v49, v52, v47
	v_fma_f32 v46, -v46, v49, v48
	v_div_fmas_f32 v46, v46, v47, v49
	ds_read2_b32 v[48:49], v6 offset1:33
	v_div_fixup_f32 v46, v46, v0, s2
	v_cmp_lt_f32_e32 vcc, 0, v0
	ds_read2_b32 v[52:53], v6 offset0:66 offset1:99
	v_readlane_b32 s28, v252, 44
	v_cndmask_b32_e32 v0, 0, v46, vcc
	s_waitcnt lgkmcnt(1)
	v_mul_f32_e32 v48, v48, v0
	v_rndne_f32_e32 v48, v48
	v_cvt_i32_f32_e32 v54, v48
	v_mul_f32_e32 v48, v0, v49
	v_rndne_f32_e32 v48, v48
	v_cvt_i32_f32_e32 v55, v48
	s_waitcnt lgkmcnt(0)
	v_mul_f32_e32 v48, v0, v52
	v_rndne_f32_e32 v48, v48
	v_cvt_i32_f32_sdwa v52, v48 dst_sel:WORD_1 dst_unused:UNUSED_PAD src0_sel:DWORD
	v_mul_f32_e32 v48, v0, v53
	v_or_b32_e32 v46, s33, v37
	v_rndne_f32_e32 v48, v48
	v_ashrrev_i32_e32 v47, 31, v46
	v_cvt_i32_f32_sdwa v53, v48 dst_sel:BYTE_3 dst_unused:UNUSED_PAD src0_sel:DWORD
	ds_read2_b32 v[48:49], v6 offset0:132 offset1:165
	v_lshlrev_b64 v[46:47], 10, v[46:47]
	v_lshl_add_u64 v[46:47], s[0:1], 0, v[46:47]
	v_lshlrev_b32_e32 v55, 8, v55
	s_mov_b32 s0, 0xc0c0500
	v_perm_b32 v54, v55, v54, s0
	v_and_b32_e32 v52, 0xff0000, v52
	v_or3_b32 v52, v54, v52, v53
	ds_read2_b32 v[54:55], v6 offset0:198 offset1:231
	s_waitcnt lgkmcnt(1)
	v_mul_f32_e32 v48, v0, v48
	v_rndne_f32_e32 v48, v48
	v_cvt_i32_f32_e32 v53, v48
	v_mul_f32_e32 v48, v0, v49
	v_rndne_f32_e32 v48, v48
	v_cvt_i32_f32_e32 v56, v48
	s_waitcnt lgkmcnt(0)
	v_mul_f32_e32 v48, v0, v54
	v_rndne_f32_e32 v48, v48
	v_cvt_i32_f32_sdwa v54, v48 dst_sel:WORD_1 dst_unused:UNUSED_PAD src0_sel:DWORD
	v_mul_f32_e32 v48, v0, v55
	v_rndne_f32_e32 v48, v48
	v_cvt_i32_f32_sdwa v55, v48 dst_sel:BYTE_3 dst_unused:UNUSED_PAD src0_sel:DWORD
	ds_read2_b32 v[48:49], v57 offset0:8 offset1:41
	v_lshlrev_b32_e32 v56, 8, v56
	v_perm_b32 v53, v56, v53, s0
	v_and_b32_e32 v54, 0xff0000, v54
	v_or3_b32 v53, v53, v54, v55
	ds_read2_b32 v[54:55], v57 offset0:74 offset1:107
	s_waitcnt lgkmcnt(1)
	v_mul_f32_e32 v48, v0, v48
	v_rndne_f32_e32 v48, v48
	v_cvt_i32_f32_e32 v56, v48
	v_mul_f32_e32 v48, v0, v49
	v_rndne_f32_e32 v48, v48
	v_cvt_i32_f32_e32 v59, v48
	s_waitcnt lgkmcnt(0)
	v_mul_f32_e32 v48, v0, v54
	v_rndne_f32_e32 v48, v48
	v_cvt_i32_f32_sdwa v54, v48 dst_sel:WORD_1 dst_unused:UNUSED_PAD src0_sel:DWORD
	v_mul_f32_e32 v48, v0, v55
	v_rndne_f32_e32 v48, v48
	v_cvt_i32_f32_sdwa v55, v48 dst_sel:BYTE_3 dst_unused:UNUSED_PAD src0_sel:DWORD
	ds_read2_b32 v[48:49], v57 offset0:140 offset1:173
	v_lshlrev_b32_e32 v59, 8, v59
	v_perm_b32 v56, v59, v56, s0
	v_and_b32_e32 v54, 0xff0000, v54
	v_or3_b32 v54, v56, v54, v55
	ds_read2_b32 v[56:57], v57 offset0:206 offset1:239
	s_waitcnt lgkmcnt(1)
	v_mul_f32_e32 v48, v0, v48
	v_mul_f32_e32 v49, v0, v49
	v_rndne_f32_e32 v48, v48
	v_rndne_f32_e32 v49, v49
	v_cvt_i32_f32_e32 v55, v48
	s_waitcnt lgkmcnt(0)
	v_mul_f32_e32 v48, v0, v56
	v_cvt_i32_f32_e32 v49, v49
	v_rndne_f32_e32 v48, v48
	v_cvt_i32_f32_sdwa v56, v48 dst_sel:WORD_1 dst_unused:UNUSED_PAD src0_sel:DWORD
	v_mul_f32_e32 v48, v0, v57
	v_rndne_f32_e32 v48, v48
	v_cvt_i32_f32_sdwa v57, v48 dst_sel:BYTE_3 dst_unused:UNUSED_PAD src0_sel:DWORD
	v_lshlrev_b32_e32 v59, 8, v49
	ds_read2_b32 v[48:49], v60 offset0:16 offset1:49
	v_perm_b32 v55, v59, v55, s0
	v_and_b32_e32 v56, 0xff0000, v56
	v_lshl_add_u64 v[46:47], v[46:47], 0, v[2:3]
	v_or3_b32 v55, v55, v56, v57
	global_store_dwordx4 v[46:47], v[52:55], off
	ds_read2_b32 v[52:53], v60 offset0:82 offset1:115
	s_waitcnt lgkmcnt(1)
	v_mul_f32_e32 v48, v0, v48
	v_rndne_f32_e32 v48, v48
	v_cvt_i32_f32_e32 v54, v48
	v_mul_f32_e32 v48, v0, v49
	v_rndne_f32_e32 v48, v48
	v_cvt_i32_f32_e32 v55, v48
	s_waitcnt lgkmcnt(0)
	v_mul_f32_e32 v48, v0, v52
	v_rndne_f32_e32 v48, v48
	v_cvt_i32_f32_sdwa v52, v48 dst_sel:WORD_1 dst_unused:UNUSED_PAD src0_sel:DWORD
	v_mul_f32_e32 v48, v0, v53
	v_rndne_f32_e32 v48, v48
	v_cvt_i32_f32_sdwa v53, v48 dst_sel:BYTE_3 dst_unused:UNUSED_PAD src0_sel:DWORD
	ds_read2_b32 v[48:49], v60 offset0:148 offset1:181
	v_lshlrev_b32_e32 v55, 8, v55
	v_perm_b32 v54, v55, v54, s0
	v_and_b32_e32 v52, 0xff0000, v52
	v_or3_b32 v52, v54, v52, v53
	ds_read2_b32 v[54:55], v60 offset0:214 offset1:247
	s_waitcnt lgkmcnt(1)
	v_mul_f32_e32 v48, v0, v48
	v_rndne_f32_e32 v48, v48
	v_cvt_i32_f32_e32 v53, v48
	v_mul_f32_e32 v48, v0, v49
	v_rndne_f32_e32 v48, v48
	v_cvt_i32_f32_e32 v56, v48
	s_waitcnt lgkmcnt(0)
	v_mul_f32_e32 v48, v0, v54
	v_rndne_f32_e32 v48, v48
	v_cvt_i32_f32_sdwa v54, v48 dst_sel:WORD_1 dst_unused:UNUSED_PAD src0_sel:DWORD
	v_mul_f32_e32 v48, v0, v55
	v_rndne_f32_e32 v48, v48
	v_add_u32_e32 v57, 0xc00, v6
	v_cvt_i32_f32_sdwa v55, v48 dst_sel:BYTE_3 dst_unused:UNUSED_PAD src0_sel:DWORD
	ds_read2_b32 v[48:49], v57 offset0:24 offset1:57
	v_lshlrev_b32_e32 v56, 8, v56
	v_perm_b32 v53, v56, v53, s0
	v_and_b32_e32 v54, 0xff0000, v54
	v_or3_b32 v53, v53, v54, v55
	ds_read2_b32 v[54:55], v57 offset0:90 offset1:123
	s_waitcnt lgkmcnt(1)
	v_mul_f32_e32 v48, v0, v48
	v_rndne_f32_e32 v48, v48
	v_cvt_i32_f32_e32 v56, v48
	v_mul_f32_e32 v48, v0, v49
	v_rndne_f32_e32 v48, v48
	v_cvt_i32_f32_e32 v59, v48
	s_waitcnt lgkmcnt(0)
	v_mul_f32_e32 v48, v0, v54
	v_rndne_f32_e32 v48, v48
	v_cvt_i32_f32_sdwa v54, v48 dst_sel:WORD_1 dst_unused:UNUSED_PAD src0_sel:DWORD
	v_mul_f32_e32 v48, v0, v55
	v_rndne_f32_e32 v48, v48
	v_cvt_i32_f32_sdwa v55, v48 dst_sel:BYTE_3 dst_unused:UNUSED_PAD src0_sel:DWORD
	ds_read2_b32 v[48:49], v57 offset0:156 offset1:189
	v_lshlrev_b32_e32 v59, 8, v59
	v_perm_b32 v56, v59, v56, s0
	v_and_b32_e32 v54, 0xff0000, v54
	v_or3_b32 v54, v56, v54, v55
	ds_read2_b32 v[56:57], v57 offset0:222 offset1:255
	s_waitcnt lgkmcnt(1)
	v_mul_f32_e32 v48, v0, v48
	v_mul_f32_e32 v49, v0, v49
	v_rndne_f32_e32 v48, v48
	v_rndne_f32_e32 v49, v49
	v_cvt_i32_f32_e32 v55, v48
	s_waitcnt lgkmcnt(0)
	v_mul_f32_e32 v48, v0, v56
	v_cvt_i32_f32_e32 v49, v49
	v_rndne_f32_e32 v48, v48
	v_cvt_i32_f32_sdwa v56, v48 dst_sel:WORD_1 dst_unused:UNUSED_PAD src0_sel:DWORD
	v_mul_f32_e32 v48, v0, v57
	v_rndne_f32_e32 v48, v48
	v_cvt_i32_f32_sdwa v57, v48 dst_sel:BYTE_3 dst_unused:UNUSED_PAD src0_sel:DWORD
	v_add_u32_e32 v60, 0x1000, v6
	v_lshlrev_b32_e32 v59, 8, v49
	ds_read2_b32 v[48:49], v60 offset0:32 offset1:65
	v_perm_b32 v55, v59, v55, s0
	v_and_b32_e32 v56, 0xff0000, v56
	v_or3_b32 v55, v55, v56, v57
	global_store_dwordx4 v[46:47], v[52:55], off offset:16
	ds_read2_b32 v[52:53], v60 offset0:98 offset1:131
	s_waitcnt lgkmcnt(1)
	v_mul_f32_e32 v48, v0, v48
	v_rndne_f32_e32 v48, v48
	v_cvt_i32_f32_e32 v54, v48
	v_mul_f32_e32 v48, v0, v49
	v_rndne_f32_e32 v48, v48
	v_cvt_i32_f32_e32 v55, v48
	s_waitcnt lgkmcnt(0)
	v_mul_f32_e32 v48, v0, v52
	v_rndne_f32_e32 v48, v48
	v_cvt_i32_f32_sdwa v52, v48 dst_sel:WORD_1 dst_unused:UNUSED_PAD src0_sel:DWORD
	v_mul_f32_e32 v48, v0, v53
	v_rndne_f32_e32 v48, v48
	v_cvt_i32_f32_sdwa v53, v48 dst_sel:BYTE_3 dst_unused:UNUSED_PAD src0_sel:DWORD
	ds_read2_b32 v[48:49], v60 offset0:164 offset1:197
	v_lshlrev_b32_e32 v55, 8, v55
	v_perm_b32 v54, v55, v54, s0
	v_and_b32_e32 v52, 0xff0000, v52
	v_or3_b32 v52, v54, v52, v53
	v_add_u32_e32 v53, 0x1200, v6
	ds_read2_b32 v[54:55], v53 offset0:102 offset1:135
	s_waitcnt lgkmcnt(1)
	v_mul_f32_e32 v48, v0, v48
	v_rndne_f32_e32 v48, v48
	v_cvt_i32_f32_e32 v53, v48
	v_mul_f32_e32 v48, v0, v49
	v_rndne_f32_e32 v48, v48
	v_cvt_i32_f32_e32 v56, v48
	s_waitcnt lgkmcnt(0)
	v_mul_f32_e32 v48, v0, v54
	v_rndne_f32_e32 v48, v48
	v_cvt_i32_f32_sdwa v54, v48 dst_sel:WORD_1 dst_unused:UNUSED_PAD src0_sel:DWORD
	v_mul_f32_e32 v48, v0, v55
	v_rndne_f32_e32 v48, v48
	v_add_u32_e32 v57, 0x1400, v6
	v_cvt_i32_f32_sdwa v55, v48 dst_sel:BYTE_3 dst_unused:UNUSED_PAD src0_sel:DWORD
	ds_read2_b32 v[48:49], v57 offset0:40 offset1:73
	v_lshlrev_b32_e32 v56, 8, v56
	v_perm_b32 v53, v56, v53, s0
	v_and_b32_e32 v54, 0xff0000, v54
	v_or3_b32 v53, v53, v54, v55
	ds_read2_b32 v[54:55], v57 offset0:106 offset1:139
	s_waitcnt lgkmcnt(1)
	v_mul_f32_e32 v48, v0, v48
	v_rndne_f32_e32 v48, v48
	v_cvt_i32_f32_e32 v56, v48
	v_mul_f32_e32 v48, v0, v49
	v_rndne_f32_e32 v48, v48
	v_cvt_i32_f32_e32 v59, v48
	s_waitcnt lgkmcnt(0)
	v_mul_f32_e32 v48, v0, v54
	v_rndne_f32_e32 v48, v48
	v_cvt_i32_f32_sdwa v54, v48 dst_sel:WORD_1 dst_unused:UNUSED_PAD src0_sel:DWORD
	v_mul_f32_e32 v48, v0, v55
	v_rndne_f32_e32 v48, v48
	v_cvt_i32_f32_sdwa v55, v48 dst_sel:BYTE_3 dst_unused:UNUSED_PAD src0_sel:DWORD
	ds_read2_b32 v[48:49], v57 offset0:172 offset1:205
	v_lshlrev_b32_e32 v57, 8, v59
	v_perm_b32 v56, v57, v56, s0
	v_and_b32_e32 v54, 0xff0000, v54
	v_or3_b32 v54, v56, v54, v55
	v_add_u32_e32 v55, 0x1600, v6
	ds_read2_b32 v[56:57], v55 offset0:110 offset1:143
	s_waitcnt lgkmcnt(1)
	v_mul_f32_e32 v48, v0, v48
	v_mul_f32_e32 v49, v0, v49
	v_rndne_f32_e32 v48, v48
	v_rndne_f32_e32 v49, v49
	v_cvt_i32_f32_e32 v55, v48
	s_waitcnt lgkmcnt(0)
	v_mul_f32_e32 v48, v0, v56
	v_cvt_i32_f32_e32 v49, v49
	v_rndne_f32_e32 v48, v48
	v_cvt_i32_f32_sdwa v56, v48 dst_sel:WORD_1 dst_unused:UNUSED_PAD src0_sel:DWORD
	v_mul_f32_e32 v48, v0, v57
	v_rndne_f32_e32 v48, v48
	v_cvt_i32_f32_sdwa v57, v48 dst_sel:BYTE_3 dst_unused:UNUSED_PAD src0_sel:DWORD
	v_add_u32_e32 v60, 0x1800, v6
	v_lshlrev_b32_e32 v59, 8, v49
	ds_read2_b32 v[48:49], v60 offset0:48 offset1:81
	v_perm_b32 v55, v59, v55, s0
	v_and_b32_e32 v56, 0xff0000, v56
	v_or3_b32 v55, v55, v56, v57
	global_store_dwordx4 v[46:47], v[52:55], off offset:32
	ds_read2_b32 v[52:53], v60 offset0:114 offset1:147
	s_waitcnt lgkmcnt(1)
	v_mul_f32_e32 v48, v0, v48
	v_rndne_f32_e32 v48, v48
	v_cvt_i32_f32_e32 v54, v48
	v_mul_f32_e32 v48, v0, v49
	v_rndne_f32_e32 v48, v48
	v_cvt_i32_f32_e32 v55, v48
	s_waitcnt lgkmcnt(0)
	v_mul_f32_e32 v48, v0, v52
	v_rndne_f32_e32 v48, v48
	v_cvt_i32_f32_sdwa v52, v48 dst_sel:WORD_1 dst_unused:UNUSED_PAD src0_sel:DWORD
	v_mul_f32_e32 v48, v0, v53
	v_rndne_f32_e32 v48, v48
	v_cvt_i32_f32_sdwa v53, v48 dst_sel:BYTE_3 dst_unused:UNUSED_PAD src0_sel:DWORD
	ds_read2_b32 v[48:49], v60 offset0:180 offset1:213
	v_lshlrev_b32_e32 v55, 8, v55
	v_perm_b32 v54, v55, v54, s0
	v_and_b32_e32 v52, 0xff0000, v52
	v_or3_b32 v52, v54, v52, v53
	v_add_u32_e32 v53, 0x1a00, v6
	ds_read2_b32 v[54:55], v53 offset0:118 offset1:151
	s_waitcnt lgkmcnt(1)
	v_mul_f32_e32 v48, v0, v48
	v_rndne_f32_e32 v48, v48
	v_cvt_i32_f32_e32 v53, v48
	v_mul_f32_e32 v48, v0, v49
	v_rndne_f32_e32 v48, v48
	v_cvt_i32_f32_e32 v56, v48
	s_waitcnt lgkmcnt(0)
	v_mul_f32_e32 v48, v0, v54
	v_rndne_f32_e32 v48, v48
	v_cvt_i32_f32_sdwa v54, v48 dst_sel:WORD_1 dst_unused:UNUSED_PAD src0_sel:DWORD
	v_mul_f32_e32 v48, v0, v55
	v_rndne_f32_e32 v48, v48
	v_add_u32_e32 v57, 0x1c00, v6
	v_cvt_i32_f32_sdwa v55, v48 dst_sel:BYTE_3 dst_unused:UNUSED_PAD src0_sel:DWORD
	ds_read2_b32 v[48:49], v57 offset0:56 offset1:89
	v_lshlrev_b32_e32 v56, 8, v56
	v_perm_b32 v53, v56, v53, s0
	v_and_b32_e32 v54, 0xff0000, v54
	v_or3_b32 v53, v53, v54, v55
	ds_read2_b32 v[54:55], v57 offset0:122 offset1:155
	s_waitcnt lgkmcnt(1)
	v_mul_f32_e32 v48, v0, v48
	v_rndne_f32_e32 v48, v48
	v_cvt_i32_f32_e32 v56, v48
	v_mul_f32_e32 v48, v0, v49
	v_rndne_f32_e32 v48, v48
	v_cvt_i32_f32_e32 v59, v48
	s_waitcnt lgkmcnt(0)
	v_mul_f32_e32 v48, v0, v54
	v_rndne_f32_e32 v48, v48
	v_cvt_i32_f32_sdwa v54, v48 dst_sel:WORD_1 dst_unused:UNUSED_PAD src0_sel:DWORD
	v_mul_f32_e32 v48, v0, v55
	v_rndne_f32_e32 v48, v48
	v_cvt_i32_f32_sdwa v55, v48 dst_sel:BYTE_3 dst_unused:UNUSED_PAD src0_sel:DWORD
	ds_read2_b32 v[48:49], v57 offset0:188 offset1:221
	v_mul_f32_e32 v44, v0, v44
	v_rndne_f32_e32 v44, v44
	v_cvt_i32_f32_sdwa v44, v44 dst_sel:WORD_1 dst_unused:UNUSED_PAD src0_sel:DWORD
	v_lshlrev_b32_e32 v57, 8, v59
	s_waitcnt lgkmcnt(0)
	v_mul_f32_e32 v49, v0, v49
	v_mul_f32_e32 v48, v0, v48
	v_rndne_f32_e32 v49, v49
	v_rndne_f32_e32 v48, v48
	v_cvt_i32_f32_e32 v49, v49
	v_cvt_i32_f32_e32 v48, v48
	v_mul_f32_e32 v0, v0, v58
	v_rndne_f32_e32 v0, v0
	v_cvt_i32_f32_sdwa v0, v0 dst_sel:BYTE_3 dst_unused:UNUSED_PAD src0_sel:DWORD
	v_lshlrev_b32_e32 v49, 8, v49
	v_perm_b32 v56, v57, v56, s0
	v_perm_b32 v48, v49, v48, s0
	s_add_i32 s98, s98, s100
	v_and_b32_e32 v54, 0xff0000, v54
	v_and_b32_e32 v44, 0xff0000, v44
	s_mov_b32 s0, 0xfffffc00
	s_cmp_lt_u32 s98, 0x1278
	s_cselect_b32 s0, 0xfffffc00, s0
	s_cmp_lt_u32 s98, 0x11d0
	s_cselect_b32 s0, 0xfffffc00, s0
	s_cmp_lt_u32 s98, 0x10e0
	s_cselect_b32 s0, 0xfffffc00, s0
	s_cmp_lt_u32 s98, 0x1010
	s_cselect_b32 s0, 0xfffffc00, s0
	s_cmp_lt_u32 s98, 0xc60
	s_cselect_b32 s0, 0x700, s0
	s_cmp_lt_u32 s98, 0xc40
	s_cselect_b32 s0, 0x6a0, s0
	s_cmp_lt_u32 s98, 0xc00
	s_cselect_b32 s0, 0x6a0, s0
	s_cmp_lt_u32 s98, 0xb60
	s_cselect_b32 s0, 0xfffff600, s0
	s_cmp_lt_u32 s98, 0xab0
	s_cselect_b32 s0, 0x890, s0
	s_cmp_lt_u32 s98, 0xa90
	s_cselect_b32 s0, 0x770, s0
	s_cmp_lt_u32 s98, 0xa20
	s_cselect_b32 s0, 0x770, s0
	s_cmp_lt_u32 s98, 0x9b0
	s_cselect_b32 s0, 0xfffffeb0, s0
	s_cmp_lt_u32 s98, 0x880
	s_cselect_b32 s0, 0xfffffeb0, s0
	s_cmp_lt_u32 s98, 0x5b0
	s_cselect_b32 s0, 0xfffffeb0, s0
	s_cmp_lt_u32 s98, 0x460
	s_cselect_b32 s0, 0xfffffeb0, s0
	s_cmp_lt_u32 s98, 0x2b0
	s_cselect_b32 s0, 0x1070, s0
	s_cmp_lt_u32 s98, 0x290
	s_cselect_b32 s0, 0xe90, s0
	s_cmp_lt_u32 s98, 0x280
	s_cselect_b32 s0, 0xe90, s0
	s_cmp_lt_u32 s98, 0x1b0
	s_cselect_b32 s0, 0xffffff00, s0
	s_cmp_lt_u32 s98, 0x100
	s_cselect_b32 s0, 0x1200, s0
	s_cmp_lt_u32 s98, 0xe0
	s_cselect_b32 s0, 0xf60, s0
	s_add_i32 s28, s98, s0
	v_or3_b32 v54, v56, v54, v55
	v_or3_b32 v55, v48, v44, v0
	s_cmp_ge_u32 s98, s99
	global_store_dwordx4 v[46:47], v[52:55], off offset:48
	s_barrier
	s_cbranch_scc1 .LBB0_253

.LBB0_1028:
	v_readlane_b32 s98, v251, 3
	v_readlane_b32 s99, v255, 29
	s_cmp_lt_u32 s98, 48
	s_cbranch_scc1 .Lwqd_skip_M
	s_sub_i32 s98, s98, 48
	s_mov_b32 s100, 0
	s_mov_b32 s101, 0
	s_cmp_eq_u32 s99, 0
	s_cselect_b32 s100, 0xe0, s100
	s_cselect_b32 s101, 0x280, s101
	s_cmp_eq_u32 s99, 1
	s_cselect_b32 s100, 0x880, s100
	s_cselect_b32 s101, 0xa20, s101
	s_cmp_eq_u32 s99, 2
	s_cselect_b32 s100, 0x1010, s100
	s_cselect_b32 s101, 0x10e0, s101
	s_add_i32 s98, s98, s100
	s_mov_b32 s99, s101
	s_cmp_ge_u32 s98, s99
	s_cbranch_scc1 .Lwqd_skip_M
	s_movk_i32 s100, 208
	s_mov_b32 s101, 3
	v_writelane_b32 v117, s0, 0
	v_writelane_b32 v117, s1, 1
	v_writelane_b32 v117, s2, 2
	v_writelane_b32 v117, s3, 3
	v_writelane_b32 v117, s4, 4
	v_writelane_b32 v117, s5, 5
	v_writelane_b32 v117, s6, 6
	v_writelane_b32 v117, s7, 7
	v_writelane_b32 v117, s8, 8
	v_writelane_b32 v117, s9, 9
	v_writelane_b32 v117, s10, 10
	v_writelane_b32 v117, s11, 11
	v_writelane_b32 v117, s12, 12
	v_writelane_b32 v117, s13, 13
	v_writelane_b32 v117, s14, 14
	v_writelane_b32 v117, s15, 15
	v_writelane_b32 v117, s16, 16
	v_writelane_b32 v117, s17, 17
	v_writelane_b32 v117, s18, 18
	v_writelane_b32 v117, s19, 19
	v_writelane_b32 v117, s20, 20
	v_writelane_b32 v117, s21, 21
	v_writelane_b32 v117, s22, 22
	v_writelane_b32 v117, s23, 23
	v_writelane_b32 v117, s24, 24
	v_writelane_b32 v117, s25, 25
	v_writelane_b32 v117, s26, 26
	v_writelane_b32 v117, s27, 27
	v_writelane_b32 v117, s28, 28
	v_writelane_b32 v117, s29, 29
	v_writelane_b32 v117, s30, 30
	v_writelane_b32 v117, s31, 31
	v_writelane_b32 v117, s32, 32
	v_writelane_b32 v117, s33, 33
	v_writelane_b32 v117, s34, 34
	v_writelane_b32 v117, s35, 35
	v_writelane_b32 v117, s36, 36
	v_writelane_b32 v117, s37, 37
	v_writelane_b32 v117, s38, 38
	v_writelane_b32 v117, s39, 39
	v_writelane_b32 v117, s40, 40
	v_writelane_b32 v117, s41, 41
	v_writelane_b32 v117, s42, 42
	v_writelane_b32 v117, s43, 43
	v_writelane_b32 v117, s44, 44
	v_writelane_b32 v117, s45, 45
	v_writelane_b32 v117, s46, 46
	v_writelane_b32 v117, s47, 47
	v_writelane_b32 v117, s48, 48
	v_writelane_b32 v117, s49, 49
	v_writelane_b32 v117, s50, 50
	v_writelane_b32 v117, s51, 51
	v_writelane_b32 v117, s52, 52
	v_writelane_b32 v117, s53, 53
	v_writelane_b32 v117, s54, 54
	v_writelane_b32 v117, s55, 55
	v_writelane_b32 v117, s56, 56
	v_writelane_b32 v117, s57, 57
	v_writelane_b32 v117, s58, 58
	v_writelane_b32 v117, s59, 59
	v_writelane_b32 v117, s60, 60
	v_writelane_b32 v117, s61, 61
	v_writelane_b32 v117, s62, 62
	v_writelane_b32 v117, s63, 63
	v_writelane_b32 v118, s64, 0
	v_writelane_b32 v118, s65, 1
	v_writelane_b32 v118, s66, 2
	v_writelane_b32 v118, s67, 3
	v_writelane_b32 v118, s68, 4
	v_writelane_b32 v118, s69, 5
	v_writelane_b32 v118, s70, 6
	v_writelane_b32 v118, s71, 7
	v_writelane_b32 v118, s72, 8
	v_writelane_b32 v118, s73, 9
	v_writelane_b32 v118, s74, 10
	v_writelane_b32 v118, s75, 11
	v_writelane_b32 v118, s76, 12
	v_writelane_b32 v118, s77, 13
	v_writelane_b32 v118, s78, 14
	v_writelane_b32 v118, s79, 15
	v_writelane_b32 v118, s80, 16
	v_writelane_b32 v118, s81, 17
	v_writelane_b32 v118, s82, 18
	v_writelane_b32 v118, s83, 19
	v_writelane_b32 v118, s84, 20
	v_writelane_b32 v118, s85, 21
	v_writelane_b32 v118, s86, 22
	v_writelane_b32 v118, s87, 23
	v_writelane_b32 v118, s88, 24
	v_writelane_b32 v118, s89, 25
	v_writelane_b32 v118, s90, 26
	v_writelane_b32 v118, s91, 27
	v_writelane_b32 v118, s92, 28
	v_writelane_b32 v118, s93, 29
	v_writelane_b32 v118, s94, 30
	v_writelane_b32 v118, s95, 31
	v_writelane_b32 v118, s96, 32
	v_writelane_b32 v118, s97, 33
	v_mov_b32_e32 v100, v0
	v_mov_b32_e32 v101, v50
	v_mov_b32_e32 v102, v51
	v_mov_b32_e32 v103, v52
	v_mov_b32_e32 v104, v54
	v_mov_b32_e32 v105, v55
	v_mov_b32_e32 v106, v56
	v_mov_b32_e32 v107, v58
	v_mov_b32_e32 v108, v59
	v_mov_b32_e32 v109, v60
	v_mov_b32_e32 v110, v62
	v_mov_b32_e32 v111, v63
	v_mov_b32_e32 v112, v64
	v_mov_b32_e32 v113, v67
	v_mov_b32_e32 v114, v75
	v_mov_b32_e32 v115, v77
	s_branch .Lwqd_entry

.Lwqd_entry:
	v_mov_b32_e32 v50, v246
	v_mov_b32_e32 v5, 0
	v_readlane_b32 s52, v252, 26
	v_readlane_b32 s53, v252, 27
	s_mov_b32 s0, 0xfffffc00
	s_cmp_lt_u32 s98, 0x1278
	s_cselect_b32 s0, 0xfffffc00, s0
	s_cmp_lt_u32 s98, 0x11d0
	s_cselect_b32 s0, 0xfffffc00, s0
	s_cmp_lt_u32 s98, 0x10e0
	s_cselect_b32 s0, 0xfffffc00, s0
	s_cmp_lt_u32 s98, 0x1010
	s_cselect_b32 s0, 0xfffffc00, s0
	s_cmp_lt_u32 s98, 0xc60
	s_cselect_b32 s0, 0x700, s0
	s_cmp_lt_u32 s98, 0xc40
	s_cselect_b32 s0, 0x6a0, s0
	s_cmp_lt_u32 s98, 0xc00
	s_cselect_b32 s0, 0x6a0, s0
	s_cmp_lt_u32 s98, 0xb60
	s_cselect_b32 s0, 0xfffff600, s0
	s_cmp_lt_u32 s98, 0xab0
	s_cselect_b32 s0, 0x890, s0
	s_cmp_lt_u32 s98, 0xa90
	s_cselect_b32 s0, 0x770, s0
	s_cmp_lt_u32 s98, 0xa20
	s_cselect_b32 s0, 0x770, s0
	s_cmp_lt_u32 s98, 0x9b0
	s_cselect_b32 s0, 0xfffffeb0, s0
	s_cmp_lt_u32 s98, 0x880
	s_cselect_b32 s0, 0xfffffeb0, s0
	s_cmp_lt_u32 s98, 0x5b0
	s_cselect_b32 s0, 0xfffffeb0, s0
	s_cmp_lt_u32 s98, 0x460
	s_cselect_b32 s0, 0xfffffeb0, s0
	s_cmp_lt_u32 s98, 0x2b0
	s_cselect_b32 s0, 0x1070, s0
	s_cmp_lt_u32 s98, 0x290
	s_cselect_b32 s0, 0xe90, s0
	s_cmp_lt_u32 s98, 0x280
	s_cselect_b32 s0, 0xe90, s0
	s_cmp_lt_u32 s98, 0x1b0
	s_cselect_b32 s0, 0xffffff00, s0
	s_cmp_lt_u32 s98, 0x100
	s_cselect_b32 s0, 0x1200, s0
	s_cmp_lt_u32 s98, 0xe0
	s_cselect_b32 s0, 0xf60, s0
	s_add_i32 s28, s98, s0
	v_lshlrev_b32_e32 v0, 2, v50
	s_add_i32 s0, 0, 0x21000
	v_and_b32_e32 v37, 31, v50
	v_add_u32_e32 v39, s0, v0
	v_cmp_gt_i32_e64 s[0:1], 32, v50
	v_lshlrev_b32_e32 v1, 1, v50
	v_lshlrev_b32_e32 v42, 2, v37
	v_writelane_b32 v116, s0, 0
	v_ashrrev_i32_e32 v40, 3, v50
	v_and_b32_e32 v2, 0xffffffc0, v1
	v_add_u32_e32 v4, 0, v42
	v_writelane_b32 v116, s1, 1
	s_add_i32 s0, 0, 0x21800
	s_movk_i32 s2, 0x84
	v_and_b32_e32 v45, 7, v50
	v_add_u32_e32 v43, s0, v0
	v_add_u32_e32 v82, s0, v42
	v_mad_u64_u32 v[6:7], s[0:1], v2, s2, v[4:5]
	v_mul_lo_u32 v41, v40, s2
	v_lshlrev_b32_e32 v45, 4, v45
	v_add3_u32 v83, v41, v45, 0
	v_lshrrev_b32_e32 v45, 5, v50
	s_movk_i32 s0, 0x2100
	v_and_b32_e32 v35, 28, v0
	v_or_b32_e32 v0, 62, v1
	v_or_b32_e32 v1, 63, v1
	v_mul_lo_u32 v84, v45, s0
	v_mul_lo_u32 v0, v0, s2
	v_mul_lo_u32 v44, v1, s2
	v_or_b32_e32 v10, 2, v2
	v_or_b32_e32 v12, 4, v2
	v_or_b32_e32 v14, 6, v2
	v_or_b32_e32 v16, 8, v2
	v_or_b32_e32 v18, 10, v2
	v_or_b32_e32 v20, 12, v2
	v_or_b32_e32 v22, 14, v2
	v_or_b32_e32 v24, 16, v2
	v_or_b32_e32 v26, 18, v2
	v_or_b32_e32 v28, 20, v2
	v_or_b32_e32 v30, 22, v2
	v_or_b32_e32 v32, 24, v2
	v_or_b32_e32 v34, 26, v2
	v_or_b32_e32 v36, 28, v2
	v_or_b32_e32 v38, 30, v2
	v_ashrrev_i32_e32 v41, 31, v40
	v_or_b32_e32 v42, v84, v42
	v_ashrrev_i32_e32 v3, 31, v2
	v_mov_b32_e32 v8, v2
	v_mov_b32_e32 v1, v2
	v_mov_b32_e32 v5, v10
	v_mov_b32_e32 v7, v12
	v_mov_b32_e32 v9, v14
	v_mov_b32_e32 v11, v16
	v_mov_b32_e32 v13, v18
	v_mov_b32_e32 v15, v20
	v_mov_b32_e32 v17, v22
	v_mov_b32_e32 v19, v24
	v_mov_b32_e32 v21, v26
	v_mov_b32_e32 v23, v28
	v_mov_b32_e32 v25, v30
	v_mov_b32_e32 v27, v32
	v_mov_b32_e32 v29, v34
	v_mov_b32_e32 v31, v36
	v_mov_b32_e32 v33, v38
	v_lshlrev_b64 v[40:41], 2, v[40:41]
	v_add_u32_e32 v42, 0, v42
	v_mov_b32_e32 v45, 0
	v_add_u32_e32 v85, v4, v0
	v_add_u32_e32 v86, v4, v44
	s_branch .Lwqd_112
.Lwqd_111:
	s_or_b64 exec, exec, s[0:1]
	s_waitcnt lgkmcnt(0)
	s_barrier
	ds_read_b32 v0, v82
	ds_read_b32 v44, v85
	ds_read_b32 v58, v86
	s_mov_b32 s2, 0x42fe0000
	v_add_u32_e32 v57, 0x400, v6
	s_waitcnt lgkmcnt(2)
	v_div_scale_f32 v46, s[0:1], v0, v0, s2
	v_rcp_f32_e32 v47, v46
	v_readlane_b32 s0, v116, 4
	v_readlane_b32 s1, v116, 5
	v_add_u32_e32 v60, 0x800, v6
	v_fma_f32 v48, -v46, v47, 1.0
	v_fmac_f32_e32 v47, v48, v47
	v_div_scale_f32 v48, vcc, s2, v0, s2
	v_mul_f32_e32 v49, v48, v47
	v_fma_f32 v52, -v46, v49, v48
	v_fmac_f32_e32 v49, v52, v47
	v_fma_f32 v46, -v46, v49, v48
	v_div_fmas_f32 v46, v46, v47, v49
	ds_read2_b32 v[48:49], v6 offset1:33
	v_div_fixup_f32 v46, v46, v0, s2
	v_cmp_lt_f32_e32 vcc, 0, v0
	ds_read2_b32 v[52:53], v6 offset0:66 offset1:99
	v_readlane_b32 s28, v116, 2
	v_cndmask_b32_e32 v0, 0, v46, vcc
	s_waitcnt lgkmcnt(1)
	v_mul_f32_e32 v48, v48, v0
	v_rndne_f32_e32 v48, v48
	v_cvt_i32_f32_e32 v54, v48
	v_mul_f32_e32 v48, v0, v49
	v_rndne_f32_e32 v48, v48
	v_cvt_i32_f32_e32 v55, v48
	s_waitcnt lgkmcnt(0)
	v_mul_f32_e32 v48, v0, v52
	v_rndne_f32_e32 v48, v48
	v_cvt_i32_f32_sdwa v52, v48 dst_sel:WORD_1 dst_unused:UNUSED_PAD src0_sel:DWORD
	v_mul_f32_e32 v48, v0, v53
	v_or_b32_e32 v46, s33, v37
	v_rndne_f32_e32 v48, v48
	v_ashrrev_i32_e32 v47, 31, v46
	v_cvt_i32_f32_sdwa v53, v48 dst_sel:BYTE_3 dst_unused:UNUSED_PAD src0_sel:DWORD
	ds_read2_b32 v[48:49], v6 offset0:132 offset1:165
	v_lshlrev_b64 v[46:47], 10, v[46:47]
	v_lshl_add_u64 v[46:47], s[0:1], 0, v[46:47]
	v_lshlrev_b32_e32 v55, 8, v55
	s_mov_b32 s0, 0xc0c0500
	v_perm_b32 v54, v55, v54, s0
	v_and_b32_e32 v52, 0xff0000, v52
	v_or3_b32 v52, v54, v52, v53
	ds_read2_b32 v[54:55], v6 offset0:198 offset1:231
	s_waitcnt lgkmcnt(1)
	v_mul_f32_e32 v48, v0, v48
	v_rndne_f32_e32 v48, v48
	v_cvt_i32_f32_e32 v53, v48
	v_mul_f32_e32 v48, v0, v49
	v_rndne_f32_e32 v48, v48
	v_cvt_i32_f32_e32 v56, v48
	s_waitcnt lgkmcnt(0)
	v_mul_f32_e32 v48, v0, v54
	v_rndne_f32_e32 v48, v48
	v_cvt_i32_f32_sdwa v54, v48 dst_sel:WORD_1 dst_unused:UNUSED_PAD src0_sel:DWORD
	v_mul_f32_e32 v48, v0, v55
	v_rndne_f32_e32 v48, v48
	v_cvt_i32_f32_sdwa v55, v48 dst_sel:BYTE_3 dst_unused:UNUSED_PAD src0_sel:DWORD
	ds_read2_b32 v[48:49], v57 offset0:8 offset1:41
	v_lshlrev_b32_e32 v56, 8, v56
	v_perm_b32 v53, v56, v53, s0
	v_and_b32_e32 v54, 0xff0000, v54
	v_or3_b32 v53, v53, v54, v55
	ds_read2_b32 v[54:55], v57 offset0:74 offset1:107
	s_waitcnt lgkmcnt(1)
	v_mul_f32_e32 v48, v0, v48
	v_rndne_f32_e32 v48, v48
	v_cvt_i32_f32_e32 v56, v48
	v_mul_f32_e32 v48, v0, v49
	v_rndne_f32_e32 v48, v48
	v_cvt_i32_f32_e32 v59, v48
	s_waitcnt lgkmcnt(0)
	v_mul_f32_e32 v48, v0, v54
	v_rndne_f32_e32 v48, v48
	v_cvt_i32_f32_sdwa v54, v48 dst_sel:WORD_1 dst_unused:UNUSED_PAD src0_sel:DWORD
	v_mul_f32_e32 v48, v0, v55
	v_rndne_f32_e32 v48, v48
	v_cvt_i32_f32_sdwa v55, v48 dst_sel:BYTE_3 dst_unused:UNUSED_PAD src0_sel:DWORD
	ds_read2_b32 v[48:49], v57 offset0:140 offset1:173
	v_lshlrev_b32_e32 v59, 8, v59
	v_perm_b32 v56, v59, v56, s0
	v_and_b32_e32 v54, 0xff0000, v54
	v_or3_b32 v54, v56, v54, v55
	ds_read2_b32 v[56:57], v57 offset0:206 offset1:239
	s_waitcnt lgkmcnt(1)
	v_mul_f32_e32 v48, v0, v48
	v_mul_f32_e32 v49, v0, v49
	v_rndne_f32_e32 v48, v48
	v_rndne_f32_e32 v49, v49
	v_cvt_i32_f32_e32 v55, v48
	s_waitcnt lgkmcnt(0)
	v_mul_f32_e32 v48, v0, v56
	v_cvt_i32_f32_e32 v49, v49
	v_rndne_f32_e32 v48, v48
	v_cvt_i32_f32_sdwa v56, v48 dst_sel:WORD_1 dst_unused:UNUSED_PAD src0_sel:DWORD
	v_mul_f32_e32 v48, v0, v57
	v_rndne_f32_e32 v48, v48
	v_cvt_i32_f32_sdwa v57, v48 dst_sel:BYTE_3 dst_unused:UNUSED_PAD src0_sel:DWORD
	v_lshlrev_b32_e32 v59, 8, v49
	ds_read2_b32 v[48:49], v60 offset0:16 offset1:49
	v_perm_b32 v55, v59, v55, s0
	v_and_b32_e32 v56, 0xff0000, v56
	v_lshl_add_u64 v[46:47], v[46:47], 0, v[2:3]
	v_or3_b32 v55, v55, v56, v57
	global_store_dwordx4 v[46:47], v[52:55], off
	ds_read2_b32 v[52:53], v60 offset0:82 offset1:115
	s_waitcnt lgkmcnt(1)
	v_mul_f32_e32 v48, v0, v48
	v_rndne_f32_e32 v48, v48
	v_cvt_i32_f32_e32 v54, v48
	v_mul_f32_e32 v48, v0, v49
	v_rndne_f32_e32 v48, v48
	v_cvt_i32_f32_e32 v55, v48
	s_waitcnt lgkmcnt(0)
	v_mul_f32_e32 v48, v0, v52
	v_rndne_f32_e32 v48, v48
	v_cvt_i32_f32_sdwa v52, v48 dst_sel:WORD_1 dst_unused:UNUSED_PAD src0_sel:DWORD
	v_mul_f32_e32 v48, v0, v53
	v_rndne_f32_e32 v48, v48
	v_cvt_i32_f32_sdwa v53, v48 dst_sel:BYTE_3 dst_unused:UNUSED_PAD src0_sel:DWORD
	ds_read2_b32 v[48:49], v60 offset0:148 offset1:181
	v_lshlrev_b32_e32 v55, 8, v55
	v_perm_b32 v54, v55, v54, s0
	v_and_b32_e32 v52, 0xff0000, v52
	v_or3_b32 v52, v54, v52, v53
	ds_read2_b32 v[54:55], v60 offset0:214 offset1:247
	s_waitcnt lgkmcnt(1)
	v_mul_f32_e32 v48, v0, v48
	v_rndne_f32_e32 v48, v48
	v_cvt_i32_f32_e32 v53, v48
	v_mul_f32_e32 v48, v0, v49
	v_rndne_f32_e32 v48, v48
	v_cvt_i32_f32_e32 v56, v48
	s_waitcnt lgkmcnt(0)
	v_mul_f32_e32 v48, v0, v54
	v_rndne_f32_e32 v48, v48
	v_cvt_i32_f32_sdwa v54, v48 dst_sel:WORD_1 dst_unused:UNUSED_PAD src0_sel:DWORD
	v_mul_f32_e32 v48, v0, v55
	v_rndne_f32_e32 v48, v48
	v_add_u32_e32 v57, 0xc00, v6
	v_cvt_i32_f32_sdwa v55, v48 dst_sel:BYTE_3 dst_unused:UNUSED_PAD src0_sel:DWORD
	ds_read2_b32 v[48:49], v57 offset0:24 offset1:57
	v_lshlrev_b32_e32 v56, 8, v56
	v_perm_b32 v53, v56, v53, s0
	v_and_b32_e32 v54, 0xff0000, v54
	v_or3_b32 v53, v53, v54, v55
	ds_read2_b32 v[54:55], v57 offset0:90 offset1:123
	s_waitcnt lgkmcnt(1)
	v_mul_f32_e32 v48, v0, v48
	v_rndne_f32_e32 v48, v48
	v_cvt_i32_f32_e32 v56, v48
	v_mul_f32_e32 v48, v0, v49
	v_rndne_f32_e32 v48, v48
	v_cvt_i32_f32_e32 v59, v48
	s_waitcnt lgkmcnt(0)
	v_mul_f32_e32 v48, v0, v54
	v_rndne_f32_e32 v48, v48
	v_cvt_i32_f32_sdwa v54, v48 dst_sel:WORD_1 dst_unused:UNUSED_PAD src0_sel:DWORD
	v_mul_f32_e32 v48, v0, v55
	v_rndne_f32_e32 v48, v48
	v_cvt_i32_f32_sdwa v55, v48 dst_sel:BYTE_3 dst_unused:UNUSED_PAD src0_sel:DWORD
	ds_read2_b32 v[48:49], v57 offset0:156 offset1:189
	v_lshlrev_b32_e32 v59, 8, v59
	v_perm_b32 v56, v59, v56, s0
	v_and_b32_e32 v54, 0xff0000, v54
	v_or3_b32 v54, v56, v54, v55
	ds_read2_b32 v[56:57], v57 offset0:222 offset1:255
	s_waitcnt lgkmcnt(1)
	v_mul_f32_e32 v48, v0, v48
	v_mul_f32_e32 v49, v0, v49
	v_rndne_f32_e32 v48, v48
	v_rndne_f32_e32 v49, v49
	v_cvt_i32_f32_e32 v55, v48
	s_waitcnt lgkmcnt(0)
	v_mul_f32_e32 v48, v0, v56
	v_cvt_i32_f32_e32 v49, v49
	v_rndne_f32_e32 v48, v48
	v_cvt_i32_f32_sdwa v56, v48 dst_sel:WORD_1 dst_unused:UNUSED_PAD src0_sel:DWORD
	v_mul_f32_e32 v48, v0, v57
	v_rndne_f32_e32 v48, v48
	v_cvt_i32_f32_sdwa v57, v48 dst_sel:BYTE_3 dst_unused:UNUSED_PAD src0_sel:DWORD
	v_add_u32_e32 v60, 0x1000, v6
	v_lshlrev_b32_e32 v59, 8, v49
	ds_read2_b32 v[48:49], v60 offset0:32 offset1:65
	v_perm_b32 v55, v59, v55, s0
	v_and_b32_e32 v56, 0xff0000, v56
	v_or3_b32 v55, v55, v56, v57
	global_store_dwordx4 v[46:47], v[52:55], off offset:16
	ds_read2_b32 v[52:53], v60 offset0:98 offset1:131
	s_waitcnt lgkmcnt(1)
	v_mul_f32_e32 v48, v0, v48
	v_rndne_f32_e32 v48, v48
	v_cvt_i32_f32_e32 v54, v48
	v_mul_f32_e32 v48, v0, v49
	v_rndne_f32_e32 v48, v48
	v_cvt_i32_f32_e32 v55, v48
	s_waitcnt lgkmcnt(0)
	v_mul_f32_e32 v48, v0, v52
	v_rndne_f32_e32 v48, v48
	v_cvt_i32_f32_sdwa v52, v48 dst_sel:WORD_1 dst_unused:UNUSED_PAD src0_sel:DWORD
	v_mul_f32_e32 v48, v0, v53
	v_rndne_f32_e32 v48, v48
	v_cvt_i32_f32_sdwa v53, v48 dst_sel:BYTE_3 dst_unused:UNUSED_PAD src0_sel:DWORD
	ds_read2_b32 v[48:49], v60 offset0:164 offset1:197
	v_lshlrev_b32_e32 v55, 8, v55
	v_perm_b32 v54, v55, v54, s0
	v_and_b32_e32 v52, 0xff0000, v52
	v_or3_b32 v52, v54, v52, v53
	v_add_u32_e32 v53, 0x1200, v6
	ds_read2_b32 v[54:55], v53 offset0:102 offset1:135
	s_waitcnt lgkmcnt(1)
	v_mul_f32_e32 v48, v0, v48
	v_rndne_f32_e32 v48, v48
	v_cvt_i32_f32_e32 v53, v48
	v_mul_f32_e32 v48, v0, v49
	v_rndne_f32_e32 v48, v48
	v_cvt_i32_f32_e32 v56, v48
	s_waitcnt lgkmcnt(0)
	v_mul_f32_e32 v48, v0, v54
	v_rndne_f32_e32 v48, v48
	v_cvt_i32_f32_sdwa v54, v48 dst_sel:WORD_1 dst_unused:UNUSED_PAD src0_sel:DWORD
	v_mul_f32_e32 v48, v0, v55
	v_rndne_f32_e32 v48, v48
	v_add_u32_e32 v57, 0x1400, v6
	v_cvt_i32_f32_sdwa v55, v48 dst_sel:BYTE_3 dst_unused:UNUSED_PAD src0_sel:DWORD
	ds_read2_b32 v[48:49], v57 offset0:40 offset1:73
	v_lshlrev_b32_e32 v56, 8, v56
	v_perm_b32 v53, v56, v53, s0
	v_and_b32_e32 v54, 0xff0000, v54
	v_or3_b32 v53, v53, v54, v55
	ds_read2_b32 v[54:55], v57 offset0:106 offset1:139
	s_waitcnt lgkmcnt(1)
	v_mul_f32_e32 v48, v0, v48
	v_rndne_f32_e32 v48, v48
	v_cvt_i32_f32_e32 v56, v48
	v_mul_f32_e32 v48, v0, v49
	v_rndne_f32_e32 v48, v48
	v_cvt_i32_f32_e32 v59, v48
	s_waitcnt lgkmcnt(0)
	v_mul_f32_e32 v48, v0, v54
	v_rndne_f32_e32 v48, v48
	v_cvt_i32_f32_sdwa v54, v48 dst_sel:WORD_1 dst_unused:UNUSED_PAD src0_sel:DWORD
	v_mul_f32_e32 v48, v0, v55
	v_rndne_f32_e32 v48, v48
	v_cvt_i32_f32_sdwa v55, v48 dst_sel:BYTE_3 dst_unused:UNUSED_PAD src0_sel:DWORD
	ds_read2_b32 v[48:49], v57 offset0:172 offset1:205
	v_lshlrev_b32_e32 v57, 8, v59
	v_perm_b32 v56, v57, v56, s0
	v_and_b32_e32 v54, 0xff0000, v54
	v_or3_b32 v54, v56, v54, v55
	v_add_u32_e32 v55, 0x1600, v6
	ds_read2_b32 v[56:57], v55 offset0:110 offset1:143
	s_waitcnt lgkmcnt(1)
	v_mul_f32_e32 v48, v0, v48
	v_mul_f32_e32 v49, v0, v49
	v_rndne_f32_e32 v48, v48
	v_rndne_f32_e32 v49, v49
	v_cvt_i32_f32_e32 v55, v48
	s_waitcnt lgkmcnt(0)
	v_mul_f32_e32 v48, v0, v56
	v_cvt_i32_f32_e32 v49, v49
	v_rndne_f32_e32 v48, v48
	v_cvt_i32_f32_sdwa v56, v48 dst_sel:WORD_1 dst_unused:UNUSED_PAD src0_sel:DWORD
	v_mul_f32_e32 v48, v0, v57
	v_rndne_f32_e32 v48, v48
	v_cvt_i32_f32_sdwa v57, v48 dst_sel:BYTE_3 dst_unused:UNUSED_PAD src0_sel:DWORD
	v_add_u32_e32 v60, 0x1800, v6
	v_lshlrev_b32_e32 v59, 8, v49
	ds_read2_b32 v[48:49], v60 offset0:48 offset1:81
	v_perm_b32 v55, v59, v55, s0
	v_and_b32_e32 v56, 0xff0000, v56
	v_or3_b32 v55, v55, v56, v57
	global_store_dwordx4 v[46:47], v[52:55], off offset:32
	ds_read2_b32 v[52:53], v60 offset0:114 offset1:147
	s_waitcnt lgkmcnt(1)
	v_mul_f32_e32 v48, v0, v48
	v_rndne_f32_e32 v48, v48
	v_cvt_i32_f32_e32 v54, v48
	v_mul_f32_e32 v48, v0, v49
	v_rndne_f32_e32 v48, v48
	v_cvt_i32_f32_e32 v55, v48
	s_waitcnt lgkmcnt(0)
	v_mul_f32_e32 v48, v0, v52
	v_rndne_f32_e32 v48, v48
	v_cvt_i32_f32_sdwa v52, v48 dst_sel:WORD_1 dst_unused:UNUSED_PAD src0_sel:DWORD
	v_mul_f32_e32 v48, v0, v53
	v_rndne_f32_e32 v48, v48
	v_cvt_i32_f32_sdwa v53, v48 dst_sel:BYTE_3 dst_unused:UNUSED_PAD src0_sel:DWORD
	ds_read2_b32 v[48:49], v60 offset0:180 offset1:213
	v_lshlrev_b32_e32 v55, 8, v55
	v_perm_b32 v54, v55, v54, s0
	v_and_b32_e32 v52, 0xff0000, v52
	v_or3_b32 v52, v54, v52, v53
	v_add_u32_e32 v53, 0x1a00, v6
	ds_read2_b32 v[54:55], v53 offset0:118 offset1:151
	s_waitcnt lgkmcnt(1)
	v_mul_f32_e32 v48, v0, v48
	v_rndne_f32_e32 v48, v48
	v_cvt_i32_f32_e32 v53, v48
	v_mul_f32_e32 v48, v0, v49
	v_rndne_f32_e32 v48, v48
	v_cvt_i32_f32_e32 v56, v48
	s_waitcnt lgkmcnt(0)
	v_mul_f32_e32 v48, v0, v54
	v_rndne_f32_e32 v48, v48
	v_cvt_i32_f32_sdwa v54, v48 dst_sel:WORD_1 dst_unused:UNUSED_PAD src0_sel:DWORD
	v_mul_f32_e32 v48, v0, v55
	v_rndne_f32_e32 v48, v48
	v_add_u32_e32 v57, 0x1c00, v6
	v_cvt_i32_f32_sdwa v55, v48 dst_sel:BYTE_3 dst_unused:UNUSED_PAD src0_sel:DWORD
	ds_read2_b32 v[48:49], v57 offset0:56 offset1:89
	v_lshlrev_b32_e32 v56, 8, v56
	v_perm_b32 v53, v56, v53, s0
	v_and_b32_e32 v54, 0xff0000, v54
	v_or3_b32 v53, v53, v54, v55
	ds_read2_b32 v[54:55], v57 offset0:122 offset1:155
	s_waitcnt lgkmcnt(1)
	v_mul_f32_e32 v48, v0, v48
	v_rndne_f32_e32 v48, v48
	v_cvt_i32_f32_e32 v56, v48
	v_mul_f32_e32 v48, v0, v49
	v_rndne_f32_e32 v48, v48
	v_cvt_i32_f32_e32 v59, v48
	s_waitcnt lgkmcnt(0)
	v_mul_f32_e32 v48, v0, v54
	v_rndne_f32_e32 v48, v48
	v_cvt_i32_f32_sdwa v54, v48 dst_sel:WORD_1 dst_unused:UNUSED_PAD src0_sel:DWORD
	v_mul_f32_e32 v48, v0, v55
	v_rndne_f32_e32 v48, v48
	v_cvt_i32_f32_sdwa v55, v48 dst_sel:BYTE_3 dst_unused:UNUSED_PAD src0_sel:DWORD
	ds_read2_b32 v[48:49], v57 offset0:188 offset1:221
	v_mul_f32_e32 v44, v0, v44
	v_rndne_f32_e32 v44, v44
	v_cvt_i32_f32_sdwa v44, v44 dst_sel:WORD_1 dst_unused:UNUSED_PAD src0_sel:DWORD
	v_lshlrev_b32_e32 v57, 8, v59
	s_waitcnt lgkmcnt(0)
	v_mul_f32_e32 v49, v0, v49
	v_mul_f32_e32 v48, v0, v48
	v_rndne_f32_e32 v49, v49
	v_rndne_f32_e32 v48, v48
	v_cvt_i32_f32_e32 v49, v49
	v_cvt_i32_f32_e32 v48, v48
	v_mul_f32_e32 v0, v0, v58
	v_rndne_f32_e32 v0, v0
	v_cvt_i32_f32_sdwa v0, v0 dst_sel:BYTE_3 dst_unused:UNUSED_PAD src0_sel:DWORD
	v_lshlrev_b32_e32 v49, 8, v49
	v_perm_b32 v56, v57, v56, s0
	v_perm_b32 v48, v49, v48, s0
	s_add_i32 s98, s98, s100
	v_and_b32_e32 v54, 0xff0000, v54
	v_and_b32_e32 v44, 0xff0000, v44
	s_mov_b32 s0, 0xfffffc00
	s_cmp_lt_u32 s98, 0x1278
	s_cselect_b32 s0, 0xfffffc00, s0
	s_cmp_lt_u32 s98, 0x11d0
	s_cselect_b32 s0, 0xfffffc00, s0
	s_cmp_lt_u32 s98, 0x10e0
	s_cselect_b32 s0, 0xfffffc00, s0
	s_cmp_lt_u32 s98, 0x1010
	s_cselect_b32 s0, 0xfffffc00, s0
	s_cmp_lt_u32 s98, 0xc60
	s_cselect_b32 s0, 0x700, s0
	s_cmp_lt_u32 s98, 0xc40
	s_cselect_b32 s0, 0x6a0, s0
	s_cmp_lt_u32 s98, 0xc00
	s_cselect_b32 s0, 0x6a0, s0
	s_cmp_lt_u32 s98, 0xb60
	s_cselect_b32 s0, 0xfffff600, s0
	s_cmp_lt_u32 s98, 0xab0
	s_cselect_b32 s0, 0x890, s0
	s_cmp_lt_u32 s98, 0xa90
	s_cselect_b32 s0, 0x770, s0
	s_cmp_lt_u32 s98, 0xa20
	s_cselect_b32 s0, 0x770, s0
	s_cmp_lt_u32 s98, 0x9b0
	s_cselect_b32 s0, 0xfffffeb0, s0
	s_cmp_lt_u32 s98, 0x880
	s_cselect_b32 s0, 0xfffffeb0, s0
	s_cmp_lt_u32 s98, 0x5b0
	s_cselect_b32 s0, 0xfffffeb0, s0
	s_cmp_lt_u32 s98, 0x460
	s_cselect_b32 s0, 0xfffffeb0, s0
	s_cmp_lt_u32 s98, 0x2b0
	s_cselect_b32 s0, 0x1070, s0
	s_cmp_lt_u32 s98, 0x290
	s_cselect_b32 s0, 0xe90, s0
	s_cmp_lt_u32 s98, 0x280
	s_cselect_b32 s0, 0xe90, s0
	s_cmp_lt_u32 s98, 0x1b0
	s_cselect_b32 s0, 0xffffff00, s0
	s_cmp_lt_u32 s98, 0x100
	s_cselect_b32 s0, 0x1200, s0
	s_cmp_lt_u32 s98, 0xe0
	s_cselect_b32 s0, 0xf60, s0
	s_add_i32 s28, s98, s0
	v_or3_b32 v54, v56, v54, v55
	v_or3_b32 v55, v48, v44, v0
	s_cmp_ge_u32 s98, s99
	global_store_dwordx4 v[46:47], v[52:55], off offset:48
	s_barrier
	s_cbranch_scc1 .Lwqd_exit

.LBB0_1570:
	v_readlane_b32 s99, v255, 29
	s_cmp_eq_u32 s99, 1
	s_cbranch_scc0 .Lwqd_skip_H
	s_lshl_b32 s101, s100, 2
	s_and_b32 s101, s101, 0xff
	v_readlane_b32 s98, v251, 3
	s_cmp_lt_u32 s98, s101
	s_cbranch_scc1 .Lwqd_skip_H
	s_sub_i32 s98, s98, s101
	s_sub_i32 s100, 0x100, s101
	s_add_i32 s98, s98, 0xc00
	s_mov_b32 s99, 0x1010
	s_cmp_ge_u32 s98, s99
	s_cbranch_scc1 .Lwqd_skip_H
	s_mov_b32 s101, 5
	v_writelane_b32 v117, s0, 0
	v_writelane_b32 v117, s1, 1
	v_writelane_b32 v117, s2, 2
	v_writelane_b32 v117, s3, 3
	v_writelane_b32 v117, s4, 4
	v_writelane_b32 v117, s5, 5
	v_writelane_b32 v117, s6, 6
	v_writelane_b32 v117, s7, 7
	v_writelane_b32 v117, s8, 8
	v_writelane_b32 v117, s9, 9
	v_writelane_b32 v117, s10, 10
	v_writelane_b32 v117, s11, 11
	v_writelane_b32 v117, s12, 12
	v_writelane_b32 v117, s13, 13
	v_writelane_b32 v117, s14, 14
	v_writelane_b32 v117, s15, 15
	v_writelane_b32 v117, s16, 16
	v_writelane_b32 v117, s17, 17
	v_writelane_b32 v117, s18, 18
	v_writelane_b32 v117, s19, 19
	v_writelane_b32 v117, s20, 20
	v_writelane_b32 v117, s21, 21
	v_writelane_b32 v117, s22, 22
	v_writelane_b32 v117, s23, 23
	v_writelane_b32 v117, s24, 24
	v_writelane_b32 v117, s25, 25
	v_writelane_b32 v117, s26, 26
	v_writelane_b32 v117, s27, 27
	v_writelane_b32 v117, s28, 28
	v_writelane_b32 v117, s29, 29
	v_writelane_b32 v117, s30, 30
	v_writelane_b32 v117, s31, 31
	v_writelane_b32 v117, s32, 32
	v_writelane_b32 v117, s33, 33
	v_writelane_b32 v117, s34, 34
	v_writelane_b32 v117, s35, 35
	v_writelane_b32 v117, s36, 36
	v_writelane_b32 v117, s37, 37
	v_writelane_b32 v117, s38, 38
	v_writelane_b32 v117, s39, 39
	v_writelane_b32 v117, s40, 40
	v_writelane_b32 v117, s41, 41
	v_writelane_b32 v117, s42, 42
	v_writelane_b32 v117, s43, 43
	v_writelane_b32 v117, s44, 44
	v_writelane_b32 v117, s45, 45
	v_writelane_b32 v117, s46, 46
	v_writelane_b32 v117, s47, 47
	v_writelane_b32 v117, s48, 48
	v_writelane_b32 v117, s49, 49
	v_writelane_b32 v117, s50, 50
	v_writelane_b32 v117, s51, 51
	v_writelane_b32 v117, s52, 52
	v_writelane_b32 v117, s53, 53
	v_writelane_b32 v117, s54, 54
	v_writelane_b32 v117, s55, 55
	v_writelane_b32 v117, s56, 56
	v_writelane_b32 v117, s57, 57
	v_writelane_b32 v117, s58, 58
	v_writelane_b32 v117, s59, 59
	v_writelane_b32 v117, s60, 60
	v_writelane_b32 v117, s61, 61
	v_writelane_b32 v117, s62, 62
	v_writelane_b32 v117, s63, 63
	v_writelane_b32 v118, s64, 0
	v_writelane_b32 v118, s65, 1
	v_writelane_b32 v118, s66, 2
	v_writelane_b32 v118, s67, 3
	v_writelane_b32 v118, s68, 4
	v_writelane_b32 v118, s69, 5
	v_writelane_b32 v118, s70, 6
	v_writelane_b32 v118, s71, 7
	v_writelane_b32 v118, s72, 8
	v_writelane_b32 v118, s73, 9
	v_writelane_b32 v118, s74, 10
	v_writelane_b32 v118, s75, 11
	v_writelane_b32 v118, s76, 12
	v_writelane_b32 v118, s77, 13
	v_writelane_b32 v118, s78, 14
	v_writelane_b32 v118, s79, 15
	v_writelane_b32 v118, s80, 16
	v_writelane_b32 v118, s81, 17
	v_writelane_b32 v118, s82, 18
	v_writelane_b32 v118, s83, 19
	v_writelane_b32 v118, s84, 20
	v_writelane_b32 v118, s85, 21
	v_writelane_b32 v118, s86, 22
	v_writelane_b32 v118, s87, 23
	v_writelane_b32 v118, s88, 24
	v_writelane_b32 v118, s89, 25
	v_writelane_b32 v118, s90, 26
	v_writelane_b32 v118, s91, 27
	v_writelane_b32 v118, s92, 28
	v_writelane_b32 v118, s93, 29
	v_writelane_b32 v118, s94, 30
	v_writelane_b32 v118, s95, 31
	v_writelane_b32 v118, s96, 32
	v_writelane_b32 v118, s97, 33
	v_mov_b32_e32 v100, v0
	v_mov_b32_e32 v101, v50
	v_mov_b32_e32 v102, v51
	v_mov_b32_e32 v103, v52
	v_mov_b32_e32 v104, v54
	v_mov_b32_e32 v105, v55
	v_mov_b32_e32 v106, v56
	v_mov_b32_e32 v107, v58
	v_mov_b32_e32 v108, v59
	v_mov_b32_e32 v109, v60
	v_mov_b32_e32 v110, v62
	v_mov_b32_e32 v111, v63
	v_mov_b32_e32 v112, v64
	v_mov_b32_e32 v113, v67
	v_mov_b32_e32 v114, v75
	v_mov_b32_e32 v115, v77
	s_branch .Lwqd_entry
